# accumulator zeroing removed in P1 P4 P7 P8: first-trip MFMAs take inline 0 as C (out-of-line first-touch blocks)
# baseline (speedup 1.0000x reference)
.LBB0_122:
	s_ashr_i32 s7, s6, 31
	s_lshl_b64 s[42:43], s[6:7], 18
	s_add_u32 s48, s53, s42
	s_addc_u32 s49, s54, s43
	s_and_b64 s[42:43], s[58:59], exec
	s_cselect_b32 s2, s49, s41
	s_cselect_b32 s7, s48, s40
	s_lshl_b32 s50, s37, 8
	s_or_b32 s51, s50, 0x80
	s_add_u32 s56, s40, 0x100
	s_addc_u32 s57, s41, 0
	s_mov_b32 s60, -2
	s_mov_b64 s[62:63], s[26:27]
	s_mov_b32 s61, 1
	s_branch .LBB0_124
.LBB0_123:
	s_mov_b32 s61, 0
	s_waitcnt lgkmcnt(0)
	v_mov_b32_e32 v201, v199
	v_lshl_add_u64 v[208:209], s[42:43], 0, v[198:199]
	v_lshl_add_u64 v[210:211], s[42:43], 0, v[200:201]
	s_barrier
	s_cmp_eq_u32 s60, -2
	s_cbranch_scc1 .Lnz_P1b_first
	s_setprio 1
	s_waitcnt lgkmcnt(0)
	v_mfma_f32_16x16x128_f8f6f4 v[126:129], v[18:25], v[58:65], v[126:129]
	v_mfma_f32_16x16x128_f8f6f4 v[122:125], v[26:33], v[58:65], v[122:125]
	v_mfma_f32_16x16x128_f8f6f4 v[110:113], v[18:25], v[50:57], v[110:113]
	v_mfma_f32_16x16x128_f8f6f4 v[106:109], v[26:33], v[50:57], v[106:109]
	v_mfma_f32_16x16x128_f8f6f4 v[78:81], v[18:25], v[42:49], v[78:81]
	v_mfma_f32_16x16x128_f8f6f4 v[74:77], v[26:33], v[42:49], v[74:77]
	v_mfma_f32_16x16x128_f8f6f4 v[70:73], v[18:25], v[34:41], v[70:73]
	v_mfma_f32_16x16x128_f8f6f4 v[66:69], v[26:33], v[34:41], v[66:69]
	s_setprio 0
	s_setprio 1
	v_mfma_f32_16x16x128_f8f6f4 v[118:121], v[2:9], v[58:65], v[118:121]
	v_mfma_f32_16x16x128_f8f6f4 v[114:117], v[10:17], v[58:65], v[114:117]
	v_mfma_f32_16x16x128_f8f6f4 v[94:97], v[2:9], v[50:57], v[94:97]
	v_mfma_f32_16x16x128_f8f6f4 v[90:93], v[10:17], v[50:57], v[90:93]
	v_mfma_f32_16x16x128_f8f6f4 v[98:101], v[2:9], v[42:49], v[98:101]
	v_mfma_f32_16x16x128_f8f6f4 v[102:105], v[10:17], v[42:49], v[102:105]
	v_mfma_f32_16x16x128_f8f6f4 v[82:85], v[2:9], v[34:41], v[82:85]
	v_mfma_f32_16x16x128_f8f6f4 v[86:89], v[10:17], v[34:41], v[86:89]
	s_setprio 0
.Lnz_P1b_back:
	s_barrier
	s_add_i32 s46, 0, 0x18000
	s_add_i32 s47, 0, 0x1c000
	v_add_u32_e32 v14, s46, v217
	v_add_u32_e32 v30, s47, v217
	ds_read_b128 v[2:5], v14
	ds_read_b128 v[6:9], v14 offset:16
	ds_read_b128 v[10:13], v14 offset:2048
	ds_read_b128 v[14:17], v14 offset:2064
	ds_read_b128 v[18:21], v30
	ds_read_b128 v[22:25], v30 offset:16
	ds_read_b128 v[26:29], v30 offset:2048
	ds_read_b128 v[30:33], v30 offset:2064
	s_mov_b32 m0, s83
	ds_read_b128 v[34:37], v220 offset:32768
	ds_read_b128 v[38:41], v220 offset:32784
	ds_read_b128 v[42:45], v220 offset:34816
	ds_read_b128 v[46:49], v220 offset:34832
	ds_read_b128 v[50:53], v220 offset:36864
	ds_read_b128 v[54:57], v220 offset:36880
	ds_read_b128 v[58:61], v220 offset:38912
	ds_read_b128 v[62:65], v220 offset:38928
	global_load_lds_dwordx4 v213, s[42:43]
	s_mov_b32 m0, s84
	s_nop 0
	global_load_lds_dwordx4 v214, s[42:43]
	s_waitcnt vmcnt(8)
	s_waitcnt lgkmcnt(0)
	s_barrier
	s_setprio 1
	s_waitcnt lgkmcnt(0)
	v_mfma_f32_16x16x128_f8f6f4 v[190:193], v[2:9], v[34:41], v[190:193]
	v_mfma_f32_16x16x128_f8f6f4 v[186:189], v[10:17], v[34:41], v[186:189]
	v_mfma_f32_16x16x128_f8f6f4 v[174:177], v[2:9], v[42:49], v[174:177]
	v_mfma_f32_16x16x128_f8f6f4 v[170:173], v[10:17], v[42:49], v[170:173]
	v_mfma_f32_16x16x128_f8f6f4 v[158:161], v[2:9], v[50:57], v[158:161]
	v_mfma_f32_16x16x128_f8f6f4 v[154:157], v[10:17], v[50:57], v[154:157]
	v_mfma_f32_16x16x128_f8f6f4 v[142:145], v[2:9], v[58:65], v[142:145]
	v_mfma_f32_16x16x128_f8f6f4 v[138:141], v[10:17], v[58:65], v[138:141]
	s_setprio 0
	s_setprio 1
	v_mfma_f32_16x16x128_f8f6f4 v[182:185], v[18:25], v[34:41], v[182:185]
	v_mfma_f32_16x16x128_f8f6f4 v[178:181], v[26:33], v[34:41], v[178:181]
	v_mfma_f32_16x16x128_f8f6f4 v[166:169], v[18:25], v[42:49], v[166:169]
	v_mfma_f32_16x16x128_f8f6f4 v[162:165], v[26:33], v[42:49], v[162:165]
	v_mfma_f32_16x16x128_f8f6f4 v[150:153], v[18:25], v[50:57], v[150:153]
	v_mfma_f32_16x16x128_f8f6f4 v[146:149], v[26:33], v[50:57], v[146:149]
	v_mfma_f32_16x16x128_f8f6f4 v[134:137], v[18:25], v[58:65], v[134:137]
	v_mfma_f32_16x16x128_f8f6f4 v[130:133], v[26:33], v[58:65], v[130:133]
	s_setprio 0
	s_barrier
	s_add_i32 s42, s46, s55
	v_lshl_add_u64 v[206:207], v[206:207], 0, s[30:31]
	s_mov_b32 m0, s42
	ds_read_b128 v[34:37], v220 offset:49152
	ds_read_b128 v[38:41], v220 offset:49168
	ds_read_b128 v[42:45], v220 offset:51200
	ds_read_b128 v[46:49], v220 offset:51216
	ds_read_b128 v[50:53], v220 offset:53248
	ds_read_b128 v[54:57], v220 offset:53264
	ds_read_b128 v[58:61], v220 offset:55296
	ds_read_b128 v[62:65], v220 offset:55312
	global_load_lds_dwordx4 v[206:207], off
	s_add_i32 m0, s42, 0x2000
	s_add_u32 s40, s40, 0x8080
	v_lshl_add_u64 v[204:205], v[204:205], 0, s[30:31]
	s_addc_u32 s41, s41, 0
	s_add_i32 s42, s47, s55
	global_load_lds_dwordx4 v[204:205], off
	v_lshl_add_u64 v[204:205], s[40:41], 0, v[194:195]
	s_mov_b32 m0, s42
	s_nop 0
	global_load_lds_dwordx4 v[204:205], off
	v_lshl_add_u64 v[204:205], s[40:41], 0, v[196:197]
	s_add_i32 m0, s42, 0x2000
	s_nop 0
	global_load_lds_dwordx4 v[204:205], off
	v_lshl_add_u64 v[204:205], v[208:209], 0, s[30:31]
	s_mov_b32 m0, s86
	s_nop 0
	global_load_lds_dwordx4 v[204:205], off
	v_lshl_add_u64 v[204:205], v[210:211], 0, s[30:31]
	s_mov_b32 m0, s87
	s_nop 0
	global_load_lds_dwordx4 v[204:205], off
	s_waitcnt vmcnt(8)
	s_waitcnt lgkmcnt(0)
	s_barrier
	s_setprio 1
	s_waitcnt lgkmcnt(0)
	v_mfma_f32_16x16x128_f8f6f4 v[126:129], v[2:9], v[34:41], v[126:129]
	v_mfma_f32_16x16x128_f8f6f4 v[122:125], v[10:17], v[34:41], v[122:125]
	v_mfma_f32_16x16x128_f8f6f4 v[110:113], v[2:9], v[42:49], v[110:113]
	v_mfma_f32_16x16x128_f8f6f4 v[106:109], v[10:17], v[42:49], v[106:109]
	v_mfma_f32_16x16x128_f8f6f4 v[78:81], v[2:9], v[50:57], v[78:81]
	v_mfma_f32_16x16x128_f8f6f4 v[74:77], v[10:17], v[50:57], v[74:77]
	v_mfma_f32_16x16x128_f8f6f4 v[70:73], v[2:9], v[58:65], v[70:73]
	v_mfma_f32_16x16x128_f8f6f4 v[66:69], v[10:17], v[58:65], v[66:69]
	s_setprio 0
	s_setprio 1
	v_mfma_f32_16x16x128_f8f6f4 v[118:121], v[18:25], v[34:41], v[118:121]
	v_mfma_f32_16x16x128_f8f6f4 v[114:117], v[26:33], v[34:41], v[114:117]
	v_mfma_f32_16x16x128_f8f6f4 v[94:97], v[18:25], v[42:49], v[94:97]
	v_mfma_f32_16x16x128_f8f6f4 v[90:93], v[26:33], v[42:49], v[90:93]
	v_mfma_f32_16x16x128_f8f6f4 v[98:101], v[18:25], v[50:57], v[98:101]
	v_mfma_f32_16x16x128_f8f6f4 v[102:105], v[26:33], v[50:57], v[102:105]
	v_mfma_f32_16x16x128_f8f6f4 v[82:85], v[18:25], v[58:65], v[82:85]
	v_mfma_f32_16x16x128_f8f6f4 v[86:89], v[26:33], v[58:65], v[86:89]
	s_setprio 0
	s_barrier
	s_add_i32 s60, s60, 2
	s_add_u32 s62, s62, 0x100
	s_addc_u32 s63, s63, 0
	s_add_u32 s56, s56, 0x100
	s_addc_u32 s57, s57, 0
	s_cmp_gt_u32 s60, 5
	s_cbranch_scc1 .LBB0_130

.LBB0_128:
	s_add_u32 s42, s62, 0x80
	s_addc_u32 s43, s63, 0
	s_waitcnt lgkmcnt(0)
	s_and_b64 s[40:41], s[40:41], exec
	s_cselect_b32 s43, s9, s43
	s_cselect_b32 s42, s8, s42
	s_cselect_b32 s41, s2, s57
	s_cselect_b32 s40, s7, s56
	s_barrier
	s_cmp_eq_u32 s60, -2
	s_cbranch_scc1 .Lnz_P1a_first
	s_setprio 1
	s_waitcnt lgkmcnt(0)
	v_mfma_f32_16x16x128_f8f6f4 v[190:193], v[18:25], v[58:65], v[190:193]
	v_mfma_f32_16x16x128_f8f6f4 v[186:189], v[26:33], v[58:65], v[186:189]
	v_mfma_f32_16x16x128_f8f6f4 v[174:177], v[18:25], v[50:57], v[174:177]
	v_mfma_f32_16x16x128_f8f6f4 v[170:173], v[26:33], v[50:57], v[170:173]
	v_mfma_f32_16x16x128_f8f6f4 v[158:161], v[18:25], v[42:49], v[158:161]
	v_mfma_f32_16x16x128_f8f6f4 v[154:157], v[26:33], v[42:49], v[154:157]
	v_mfma_f32_16x16x128_f8f6f4 v[142:145], v[18:25], v[34:41], v[142:145]
	v_mfma_f32_16x16x128_f8f6f4 v[138:141], v[26:33], v[34:41], v[138:141]
	s_setprio 0
	s_setprio 1
	v_mfma_f32_16x16x128_f8f6f4 v[182:185], v[2:9], v[58:65], v[182:185]
	v_mfma_f32_16x16x128_f8f6f4 v[178:181], v[10:17], v[58:65], v[178:181]
	v_mfma_f32_16x16x128_f8f6f4 v[166:169], v[2:9], v[50:57], v[166:169]
	v_mfma_f32_16x16x128_f8f6f4 v[162:165], v[10:17], v[50:57], v[162:165]
	v_mfma_f32_16x16x128_f8f6f4 v[150:153], v[2:9], v[42:49], v[150:153]
	v_mfma_f32_16x16x128_f8f6f4 v[146:149], v[10:17], v[42:49], v[146:149]
	v_mfma_f32_16x16x128_f8f6f4 v[134:137], v[2:9], v[34:41], v[134:137]
	v_mfma_f32_16x16x128_f8f6f4 v[130:133], v[10:17], v[34:41], v[130:133]
	s_setprio 0
.Lnz_P1a_back:
	s_barrier
	s_mov_b32 m0, s64
	v_lshl_add_u64 v[206:207], s[40:41], 0, v[194:195]
	s_add_u32 s68, s40, 0x8000
	ds_read_b128 v[58:61], v220 offset:16384
	ds_read_b128 v[62:65], v220 offset:16400
	ds_read_b128 v[50:53], v220 offset:18432
	ds_read_b128 v[54:57], v220 offset:18448
	ds_read_b128 v[42:45], v220 offset:20480
	ds_read_b128 v[46:49], v220 offset:20496
	ds_read_b128 v[34:37], v220 offset:22528
	ds_read_b128 v[38:41], v220 offset:22544
	global_load_lds_dwordx4 v[206:207], off
	v_lshl_add_u64 v[204:205], s[40:41], 0, v[196:197]
	s_mov_b32 m0, s65
	s_addc_u32 s69, s41, 0
	global_load_lds_dwordx4 v[204:205], off
	v_lshl_add_u64 v[208:209], s[68:69], 0, v[194:195]
	s_mov_b32 m0, s66
	s_andn2_b64 vcc, exec, s[46:47]
	global_load_lds_dwordx4 v[208:209], off
	v_lshl_add_u64 v[208:209], s[68:69], 0, v[196:197]
	s_mov_b32 m0, s67
	s_nop 0
	global_load_lds_dwordx4 v[208:209], off
	s_mov_b32 m0, s39
	s_nop 0
	global_load_lds_dwordx4 v198, s[42:43]
	s_mov_b32 m0, s78
	s_nop 0
	global_load_lds_dwordx4 v200, s[42:43]
	s_cbranch_vccnz .LBB0_123
	s_waitcnt vmcnt(8)
	s_branch .LBB0_123

.LBB0_569:
	s_ashr_i32 s9, s8, 31
	s_lshl_b64 s[30:31], s[8:9], 18
	s_add_u32 s30, s33, s30
	s_addc_u32 s31, s46, s31
	s_and_b64 s[40:41], s[36:37], exec
	s_cselect_b32 s2, s31, s39
	s_cselect_b32 s9, s30, s38
	s_lshl_b32 s35, s27, 8
	s_or_b32 s63, s35, 0x80
	s_add_u32 s64, s38, 0x100
	s_addc_u32 s65, s39, 0
	s_mov_b32 s66, -2
	s_mov_b64 s[38:39], s[18:19]
	s_waitcnt vmcnt(0)
	s_mov_b32 s67, 1
	s_branch .LBB0_571
.LBB0_570:
	s_mov_b32 s67, 0
	s_waitcnt lgkmcnt(0)
	v_mov_b32_e32 v201, v199
	v_lshl_add_u64 v[210:211], s[42:43], 0, v[198:199]
	v_lshl_add_u64 v[212:213], s[42:43], 0, v[200:201]
	s_barrier
	s_cmp_eq_u32 s66, -2
	s_cbranch_scc1 .Lnz_P4b_first
	s_setprio 1
	s_waitcnt lgkmcnt(0)
	v_mfma_f32_16x16x128_f8f6f4 v[126:129], v[18:25], v[58:65], v[126:129]
	v_mfma_f32_16x16x128_f8f6f4 v[122:125], v[26:33], v[58:65], v[122:125]
	v_mfma_f32_16x16x128_f8f6f4 v[110:113], v[18:25], v[50:57], v[110:113]
	v_mfma_f32_16x16x128_f8f6f4 v[106:109], v[26:33], v[50:57], v[106:109]
	v_mfma_f32_16x16x128_f8f6f4 v[86:89], v[18:25], v[42:49], v[86:89]
	v_mfma_f32_16x16x128_f8f6f4 v[82:85], v[26:33], v[42:49], v[82:85]
	v_mfma_f32_16x16x128_f8f6f4 v[70:73], v[18:25], v[34:41], v[70:73]
	v_mfma_f32_16x16x128_f8f6f4 v[66:69], v[26:33], v[34:41], v[66:69]
	s_setprio 0
	s_setprio 1
	v_mfma_f32_16x16x128_f8f6f4 v[118:121], v[2:9], v[58:65], v[118:121]
	v_mfma_f32_16x16x128_f8f6f4 v[114:117], v[10:17], v[58:65], v[114:117]
	v_mfma_f32_16x16x128_f8f6f4 v[102:105], v[2:9], v[50:57], v[102:105]
	v_mfma_f32_16x16x128_f8f6f4 v[90:93], v[10:17], v[50:57], v[90:93]
	v_mfma_f32_16x16x128_f8f6f4 v[98:101], v[2:9], v[42:49], v[98:101]
	v_mfma_f32_16x16x128_f8f6f4 v[94:97], v[10:17], v[42:49], v[94:97]
	v_mfma_f32_16x16x128_f8f6f4 v[78:81], v[2:9], v[34:41], v[78:81]
	v_mfma_f32_16x16x128_f8f6f4 v[74:77], v[10:17], v[34:41], v[74:77]
	s_setprio 0
.Lnz_P4b_back:
	s_barrier
	s_add_i32 s44, 0, 0x18000
	s_add_i32 s45, 0, 0x1c000
	v_add_u32_e32 v14, s44, v220
	v_add_u32_e32 v30, s45, v220
	ds_read_b128 v[2:5], v14
	ds_read_b128 v[6:9], v14 offset:16
	ds_read_b128 v[10:13], v14 offset:2048
	ds_read_b128 v[14:17], v14 offset:2064
	ds_read_b128 v[18:21], v30
	ds_read_b128 v[22:25], v30 offset:16
	ds_read_b128 v[26:29], v30 offset:2048
	ds_read_b128 v[30:33], v30 offset:2064
	s_mov_b32 m0, s55
	ds_read_b128 v[34:37], v225 offset:32768
	ds_read_b128 v[38:41], v225 offset:32784
	ds_read_b128 v[42:45], v225 offset:34816
	ds_read_b128 v[46:49], v225 offset:34832
	ds_read_b128 v[50:53], v225 offset:36864
	ds_read_b128 v[54:57], v225 offset:36880
	ds_read_b128 v[58:61], v225 offset:38912
	ds_read_b128 v[62:65], v225 offset:38928
	global_load_lds_dwordx4 v217, s[42:43]
	s_mov_b32 m0, s58
	s_nop 0
	global_load_lds_dwordx4 v218, s[42:43]
	s_waitcnt vmcnt(8)
	s_waitcnt lgkmcnt(0)
	s_barrier
	s_setprio 1
	s_waitcnt lgkmcnt(0)
	v_mfma_f32_16x16x128_f8f6f4 v[190:193], v[2:9], v[34:41], v[190:193]
	v_mfma_f32_16x16x128_f8f6f4 v[186:189], v[10:17], v[34:41], v[186:189]
	v_mfma_f32_16x16x128_f8f6f4 v[174:177], v[2:9], v[42:49], v[174:177]
	v_mfma_f32_16x16x128_f8f6f4 v[170:173], v[10:17], v[42:49], v[170:173]
	v_mfma_f32_16x16x128_f8f6f4 v[158:161], v[2:9], v[50:57], v[158:161]
	v_mfma_f32_16x16x128_f8f6f4 v[154:157], v[10:17], v[50:57], v[154:157]
	v_mfma_f32_16x16x128_f8f6f4 v[142:145], v[2:9], v[58:65], v[142:145]
	v_mfma_f32_16x16x128_f8f6f4 v[138:141], v[10:17], v[58:65], v[138:141]
	s_setprio 0
	s_setprio 1
	v_mfma_f32_16x16x128_f8f6f4 v[182:185], v[18:25], v[34:41], v[182:185]
	v_mfma_f32_16x16x128_f8f6f4 v[178:181], v[26:33], v[34:41], v[178:181]
	v_mfma_f32_16x16x128_f8f6f4 v[166:169], v[18:25], v[42:49], v[166:169]
	v_mfma_f32_16x16x128_f8f6f4 v[162:165], v[26:33], v[42:49], v[162:165]
	v_mfma_f32_16x16x128_f8f6f4 v[150:153], v[18:25], v[50:57], v[150:153]
	v_mfma_f32_16x16x128_f8f6f4 v[146:149], v[26:33], v[50:57], v[146:149]
	v_mfma_f32_16x16x128_f8f6f4 v[134:137], v[18:25], v[58:65], v[134:137]
	v_mfma_f32_16x16x128_f8f6f4 v[130:133], v[26:33], v[58:65], v[130:133]
	s_setprio 0
	s_barrier
	s_add_i32 s42, s44, s47
	v_lshl_add_u64 v[208:209], v[208:209], 0, s[20:21]
	s_mov_b32 m0, s42
	ds_read_b128 v[34:37], v225 offset:49152
	ds_read_b128 v[38:41], v225 offset:49168
	ds_read_b128 v[42:45], v225 offset:51200
	ds_read_b128 v[46:49], v225 offset:51216
	ds_read_b128 v[50:53], v225 offset:53248
	ds_read_b128 v[54:57], v225 offset:53264
	ds_read_b128 v[58:61], v225 offset:55296
	ds_read_b128 v[62:65], v225 offset:55312
	global_load_lds_dwordx4 v[208:209], off
	s_add_i32 m0, s42, 0x2000
	s_add_u32 s40, s40, 0x8080
	v_lshl_add_u64 v[206:207], v[206:207], 0, s[20:21]
	s_addc_u32 s41, s41, 0
	s_add_i32 s42, s45, s47
	global_load_lds_dwordx4 v[206:207], off
	v_lshl_add_u64 v[206:207], s[40:41], 0, v[194:195]
	s_mov_b32 m0, s42
	s_nop 0
	global_load_lds_dwordx4 v[206:207], off
	v_lshl_add_u64 v[206:207], s[40:41], 0, v[196:197]
	s_add_i32 m0, s42, 0x2000
	s_nop 0
	global_load_lds_dwordx4 v[206:207], off
	v_lshl_add_u64 v[206:207], v[210:211], 0, s[20:21]
	s_mov_b32 m0, s60
	s_nop 0
	global_load_lds_dwordx4 v[206:207], off
	v_lshl_add_u64 v[206:207], v[212:213], 0, s[20:21]
	s_mov_b32 m0, s61
	s_nop 0
	global_load_lds_dwordx4 v[206:207], off
	s_waitcnt vmcnt(8)
	s_waitcnt lgkmcnt(0)
	s_barrier
	s_setprio 1
	s_waitcnt lgkmcnt(0)
	v_mfma_f32_16x16x128_f8f6f4 v[126:129], v[2:9], v[34:41], v[126:129]
	v_mfma_f32_16x16x128_f8f6f4 v[122:125], v[10:17], v[34:41], v[122:125]
	v_mfma_f32_16x16x128_f8f6f4 v[110:113], v[2:9], v[42:49], v[110:113]
	v_mfma_f32_16x16x128_f8f6f4 v[106:109], v[10:17], v[42:49], v[106:109]
	v_mfma_f32_16x16x128_f8f6f4 v[86:89], v[2:9], v[50:57], v[86:89]
	v_mfma_f32_16x16x128_f8f6f4 v[82:85], v[10:17], v[50:57], v[82:85]
	v_mfma_f32_16x16x128_f8f6f4 v[70:73], v[2:9], v[58:65], v[70:73]
	v_mfma_f32_16x16x128_f8f6f4 v[66:69], v[10:17], v[58:65], v[66:69]
	s_setprio 0
	s_setprio 1
	v_mfma_f32_16x16x128_f8f6f4 v[118:121], v[18:25], v[34:41], v[118:121]
	v_mfma_f32_16x16x128_f8f6f4 v[114:117], v[26:33], v[34:41], v[114:117]
	v_mfma_f32_16x16x128_f8f6f4 v[102:105], v[18:25], v[42:49], v[102:105]
	v_mfma_f32_16x16x128_f8f6f4 v[90:93], v[26:33], v[42:49], v[90:93]
	v_mfma_f32_16x16x128_f8f6f4 v[98:101], v[18:25], v[50:57], v[98:101]
	v_mfma_f32_16x16x128_f8f6f4 v[94:97], v[26:33], v[50:57], v[94:97]
	v_mfma_f32_16x16x128_f8f6f4 v[78:81], v[18:25], v[58:65], v[78:81]
	v_mfma_f32_16x16x128_f8f6f4 v[74:77], v[26:33], v[58:65], v[74:77]
	s_setprio 0
	s_barrier
	s_add_i32 s66, s66, 2
	s_add_u32 s38, s38, 0x100
	s_addc_u32 s39, s39, 0
	s_add_u32 s64, s64, 0x100
	s_addc_u32 s65, s65, 0
	s_cmp_gt_u32 s66, 5
	s_cbranch_scc1 .LBB0_577

.LBB0_575:
	s_add_u32 s42, s38, 0x80
	s_addc_u32 s43, s39, 0
	s_waitcnt lgkmcnt(0)
	s_and_b64 s[40:41], s[40:41], exec
	s_cselect_b32 s43, s11, s43
	s_cselect_b32 s42, s10, s42
	s_cselect_b32 s41, s2, s65
	s_cselect_b32 s40, s9, s64
	s_barrier
	s_cmp_eq_u32 s66, -2
	s_cbranch_scc1 .Lnz_P4a_first
	s_setprio 1
	s_waitcnt lgkmcnt(0)
	v_mfma_f32_16x16x128_f8f6f4 v[190:193], v[18:25], v[58:65], v[190:193]
	v_mfma_f32_16x16x128_f8f6f4 v[186:189], v[26:33], v[58:65], v[186:189]
	v_mfma_f32_16x16x128_f8f6f4 v[174:177], v[18:25], v[50:57], v[174:177]
	v_mfma_f32_16x16x128_f8f6f4 v[170:173], v[26:33], v[50:57], v[170:173]
	v_mfma_f32_16x16x128_f8f6f4 v[158:161], v[18:25], v[42:49], v[158:161]
	v_mfma_f32_16x16x128_f8f6f4 v[154:157], v[26:33], v[42:49], v[154:157]
	v_mfma_f32_16x16x128_f8f6f4 v[142:145], v[18:25], v[34:41], v[142:145]
	v_mfma_f32_16x16x128_f8f6f4 v[138:141], v[26:33], v[34:41], v[138:141]
	s_setprio 0
	s_setprio 1
	v_mfma_f32_16x16x128_f8f6f4 v[182:185], v[2:9], v[58:65], v[182:185]
	v_mfma_f32_16x16x128_f8f6f4 v[178:181], v[10:17], v[58:65], v[178:181]
	v_mfma_f32_16x16x128_f8f6f4 v[166:169], v[2:9], v[50:57], v[166:169]
	v_mfma_f32_16x16x128_f8f6f4 v[162:165], v[10:17], v[50:57], v[162:165]
	v_mfma_f32_16x16x128_f8f6f4 v[150:153], v[2:9], v[42:49], v[150:153]
	v_mfma_f32_16x16x128_f8f6f4 v[146:149], v[10:17], v[42:49], v[146:149]
	v_mfma_f32_16x16x128_f8f6f4 v[134:137], v[2:9], v[34:41], v[134:137]
	v_mfma_f32_16x16x128_f8f6f4 v[130:133], v[10:17], v[34:41], v[130:133]
	s_setprio 0
.Lnz_P4a_back:
	s_barrier
	s_mov_b32 m0, s49
	v_lshl_add_u64 v[208:209], s[40:41], 0, v[194:195]
	s_add_u32 s68, s40, 0x8000
	ds_read_b128 v[58:61], v225 offset:16384
	ds_read_b128 v[62:65], v225 offset:16400
	ds_read_b128 v[50:53], v225 offset:18432
	ds_read_b128 v[54:57], v225 offset:18448
	ds_read_b128 v[42:45], v225 offset:20480
	ds_read_b128 v[46:49], v225 offset:20496
	ds_read_b128 v[34:37], v225 offset:22528
	ds_read_b128 v[38:41], v225 offset:22544
	global_load_lds_dwordx4 v[208:209], off
	v_lshl_add_u64 v[206:207], s[40:41], 0, v[196:197]
	s_mov_b32 m0, s50
	s_addc_u32 s69, s41, 0
	global_load_lds_dwordx4 v[206:207], off
	v_lshl_add_u64 v[210:211], s[68:69], 0, v[194:195]
	s_mov_b32 m0, s51
	s_andn2_b64 vcc, exec, s[44:45]
	global_load_lds_dwordx4 v[210:211], off
	v_lshl_add_u64 v[210:211], s[68:69], 0, v[196:197]
	s_mov_b32 m0, s53
	s_nop 0
	global_load_lds_dwordx4 v[210:211], off
	s_mov_b32 m0, s48
	s_nop 0
	global_load_lds_dwordx4 v198, s[42:43]
	s_mov_b32 m0, s54
	s_nop 0
	global_load_lds_dwordx4 v200, s[42:43]
	s_cbranch_vccnz .LBB0_570
	s_waitcnt vmcnt(8)
	s_branch .LBB0_570

.LBB0_984:
	s_ashr_i32 s11, s10, 31
	s_lshl_b64 s[30:31], s[10:11], 18
	s_add_u32 s30, s40, s30
	s_addc_u32 s31, s41, s31
	s_and_b64 s[46:47], s[36:37], exec
	s_cselect_b32 s2, s31, s39
	s_cselect_b32 s11, s30, s38
	s_xor_b32 s44, s44, 0x400
	s_add_i32 s82, s44, 0
	s_add_i32 s82, s82, 0x23400
	s_add_u32 s85, s38, 0x100
	s_addc_u32 s86, s39, 0
	s_mov_b32 s87, -2
	s_mov_b64 s[38:39], s[18:19]
	s_mov_b32 s88, 1
	s_branch .LBB0_986
.LBB0_985:
	s_mov_b32 s88, 0
	s_waitcnt lgkmcnt(0)
	v_mov_b32_e32 v201, v199
	v_lshl_add_u64 v[210:211], s[46:47], 0, v[198:199]
	v_lshl_add_u64 v[212:213], s[46:47], 0, v[200:201]
	s_barrier
	s_cmp_eq_u32 s87, -2
	s_cbranch_scc1 .Lnz_P7b_first
	s_setprio 1
	s_waitcnt lgkmcnt(0)
	v_mfma_f32_16x16x128_f8f6f4 v[126:129], v[18:25], v[58:65], v[126:129]
	v_mfma_f32_16x16x128_f8f6f4 v[122:125], v[26:33], v[58:65], v[122:125]
	v_mfma_f32_16x16x128_f8f6f4 v[110:113], v[18:25], v[50:57], v[110:113]
	v_mfma_f32_16x16x128_f8f6f4 v[106:109], v[26:33], v[50:57], v[106:109]
	v_mfma_f32_16x16x128_f8f6f4 v[86:89], v[18:25], v[42:49], v[86:89]
	v_mfma_f32_16x16x128_f8f6f4 v[82:85], v[26:33], v[42:49], v[82:85]
	v_mfma_f32_16x16x128_f8f6f4 v[70:73], v[18:25], v[34:41], v[70:73]
	v_mfma_f32_16x16x128_f8f6f4 v[66:69], v[26:33], v[34:41], v[66:69]
	s_setprio 0
	s_setprio 1
	v_mfma_f32_16x16x128_f8f6f4 v[118:121], v[2:9], v[58:65], v[118:121]
	v_mfma_f32_16x16x128_f8f6f4 v[114:117], v[10:17], v[58:65], v[114:117]
	v_mfma_f32_16x16x128_f8f6f4 v[102:105], v[2:9], v[50:57], v[102:105]
	v_mfma_f32_16x16x128_f8f6f4 v[90:93], v[10:17], v[50:57], v[90:93]
	v_mfma_f32_16x16x128_f8f6f4 v[94:97], v[2:9], v[42:49], v[94:97]
	v_mfma_f32_16x16x128_f8f6f4 v[98:101], v[10:17], v[42:49], v[98:101]
	v_mfma_f32_16x16x128_f8f6f4 v[74:77], v[2:9], v[34:41], v[74:77]
	v_mfma_f32_16x16x128_f8f6f4 v[78:81], v[10:17], v[34:41], v[78:81]
	s_setprio 0
.Lnz_P7b_back:
	s_barrier
	s_add_i32 s48, 0, 0x18000
	s_add_i32 s49, 0, 0x1c000
	v_add_u32_e32 v14, s48, v217
	v_add_u32_e32 v30, s49, v217
	ds_read_b128 v[2:5], v14
	ds_read_b128 v[6:9], v14 offset:16
	ds_read_b128 v[10:13], v14 offset:2048
	ds_read_b128 v[14:17], v14 offset:2064
	ds_read_b128 v[18:21], v30
	ds_read_b128 v[22:25], v30 offset:16
	ds_read_b128 v[26:29], v30 offset:2048
	ds_read_b128 v[30:33], v30 offset:2064
	s_mov_b32 m0, s65
	ds_read_b128 v[34:37], v222 offset:32768
	ds_read_b128 v[38:41], v222 offset:32784
	ds_read_b128 v[42:45], v222 offset:34816
	ds_read_b128 v[46:49], v222 offset:34832
	ds_read_b128 v[50:53], v222 offset:36864
	ds_read_b128 v[54:57], v222 offset:36880
	ds_read_b128 v[58:61], v222 offset:38912
	ds_read_b128 v[62:65], v222 offset:38928
	global_load_lds_dwordx4 v215, s[46:47]
	s_mov_b32 m0, s66
	s_nop 0
	global_load_lds_dwordx4 v216, s[46:47]
	s_waitcnt vmcnt(8)
	s_waitcnt lgkmcnt(0)
	s_barrier
	s_setprio 1
	s_waitcnt lgkmcnt(0)
	v_mfma_f32_16x16x128_f8f6f4 v[190:193], v[2:9], v[34:41], v[190:193]
	v_mfma_f32_16x16x128_f8f6f4 v[186:189], v[10:17], v[34:41], v[186:189]
	v_mfma_f32_16x16x128_f8f6f4 v[174:177], v[2:9], v[42:49], v[174:177]
	v_mfma_f32_16x16x128_f8f6f4 v[170:173], v[10:17], v[42:49], v[170:173]
	v_mfma_f32_16x16x128_f8f6f4 v[158:161], v[2:9], v[50:57], v[158:161]
	v_mfma_f32_16x16x128_f8f6f4 v[154:157], v[10:17], v[50:57], v[154:157]
	v_mfma_f32_16x16x128_f8f6f4 v[142:145], v[2:9], v[58:65], v[142:145]
	v_mfma_f32_16x16x128_f8f6f4 v[138:141], v[10:17], v[58:65], v[138:141]
	s_setprio 0
	s_setprio 1
	v_mfma_f32_16x16x128_f8f6f4 v[182:185], v[18:25], v[34:41], v[182:185]
	v_mfma_f32_16x16x128_f8f6f4 v[178:181], v[26:33], v[34:41], v[178:181]
	v_mfma_f32_16x16x128_f8f6f4 v[166:169], v[18:25], v[42:49], v[166:169]
	v_mfma_f32_16x16x128_f8f6f4 v[162:165], v[26:33], v[42:49], v[162:165]
	v_mfma_f32_16x16x128_f8f6f4 v[150:153], v[18:25], v[50:57], v[150:153]
	v_mfma_f32_16x16x128_f8f6f4 v[146:149], v[26:33], v[50:57], v[146:149]
	v_mfma_f32_16x16x128_f8f6f4 v[134:137], v[18:25], v[58:65], v[134:137]
	v_mfma_f32_16x16x128_f8f6f4 v[130:133], v[26:33], v[58:65], v[130:133]
	s_setprio 0
	s_barrier
	s_add_i32 s46, s48, s52
	v_lshl_add_u64 v[208:209], v[208:209], 0, s[20:21]
	s_mov_b32 m0, s46
	ds_read_b128 v[34:37], v222 offset:49152
	ds_read_b128 v[38:41], v222 offset:49168
	ds_read_b128 v[42:45], v222 offset:51200
	ds_read_b128 v[46:49], v222 offset:51216
	ds_read_b128 v[50:53], v222 offset:53248
	ds_read_b128 v[54:57], v222 offset:53264
	ds_read_b128 v[58:61], v222 offset:55296
	ds_read_b128 v[62:65], v222 offset:55312
	global_load_lds_dwordx4 v[208:209], off
	s_add_i32 m0, s46, 0x2000
	s_add_u32 s44, s44, 0x20080
	v_lshl_add_u64 v[206:207], v[206:207], 0, s[20:21]
	s_addc_u32 s45, s45, 0
	s_add_i32 s46, s49, s52
	global_load_lds_dwordx4 v[206:207], off
	v_lshl_add_u64 v[206:207], s[44:45], 0, v[194:195]
	s_mov_b32 m0, s46
	s_nop 0
	global_load_lds_dwordx4 v[206:207], off
	v_lshl_add_u64 v[206:207], s[44:45], 0, v[196:197]
	s_add_i32 m0, s46, 0x2000
	s_nop 0
	global_load_lds_dwordx4 v[206:207], off
	v_lshl_add_u64 v[206:207], v[210:211], 0, s[20:21]
	s_mov_b32 m0, s68
	s_nop 0
	global_load_lds_dwordx4 v[206:207], off
	v_lshl_add_u64 v[206:207], v[212:213], 0, s[20:21]
	s_mov_b32 m0, s69
	s_nop 0
	global_load_lds_dwordx4 v[206:207], off
	s_waitcnt vmcnt(8)
	s_waitcnt lgkmcnt(0)
	s_barrier
	s_setprio 1
	s_waitcnt lgkmcnt(0)
	v_mfma_f32_16x16x128_f8f6f4 v[126:129], v[2:9], v[34:41], v[126:129]
	v_mfma_f32_16x16x128_f8f6f4 v[122:125], v[10:17], v[34:41], v[122:125]
	v_mfma_f32_16x16x128_f8f6f4 v[110:113], v[2:9], v[42:49], v[110:113]
	v_mfma_f32_16x16x128_f8f6f4 v[106:109], v[10:17], v[42:49], v[106:109]
	v_mfma_f32_16x16x128_f8f6f4 v[86:89], v[2:9], v[50:57], v[86:89]
	v_mfma_f32_16x16x128_f8f6f4 v[82:85], v[10:17], v[50:57], v[82:85]
	v_mfma_f32_16x16x128_f8f6f4 v[70:73], v[2:9], v[58:65], v[70:73]
	v_mfma_f32_16x16x128_f8f6f4 v[66:69], v[10:17], v[58:65], v[66:69]
	s_setprio 0
	s_setprio 1
	v_mfma_f32_16x16x128_f8f6f4 v[118:121], v[18:25], v[34:41], v[118:121]
	v_mfma_f32_16x16x128_f8f6f4 v[114:117], v[26:33], v[34:41], v[114:117]
	v_mfma_f32_16x16x128_f8f6f4 v[102:105], v[18:25], v[42:49], v[102:105]
	v_mfma_f32_16x16x128_f8f6f4 v[90:93], v[26:33], v[42:49], v[90:93]
	v_mfma_f32_16x16x128_f8f6f4 v[94:97], v[18:25], v[50:57], v[94:97]
	v_mfma_f32_16x16x128_f8f6f4 v[98:101], v[26:33], v[50:57], v[98:101]
	v_mfma_f32_16x16x128_f8f6f4 v[74:77], v[18:25], v[58:65], v[74:77]
	v_mfma_f32_16x16x128_f8f6f4 v[78:81], v[26:33], v[58:65], v[78:81]
	s_setprio 0
	s_barrier
	s_add_i32 s87, s87, 2
	s_add_u32 s38, s38, 0x100
	s_addc_u32 s39, s39, 0
	s_add_u32 s85, s85, 0x100
	s_addc_u32 s86, s86, 0
	s_cmp_gt_u32 s87, 5
	s_cbranch_scc1 .LBB0_992

.LBB0_990:
	s_add_u32 s46, s38, 0x80
	s_addc_u32 s47, s39, 0
	s_waitcnt lgkmcnt(0)
	s_and_b64 s[44:45], s[44:45], exec
	s_cselect_b32 s47, s15, s47
	s_cselect_b32 s46, s14, s46
	s_cselect_b32 s45, s2, s86
	s_cselect_b32 s44, s11, s85
	s_barrier
	s_cmp_eq_u32 s87, -2
	s_cbranch_scc1 .Lnz_P7a_first
	s_setprio 1
	s_waitcnt lgkmcnt(0)
	v_mfma_f32_16x16x128_f8f6f4 v[190:193], v[18:25], v[58:65], v[190:193]
	v_mfma_f32_16x16x128_f8f6f4 v[186:189], v[26:33], v[58:65], v[186:189]
	v_mfma_f32_16x16x128_f8f6f4 v[174:177], v[18:25], v[50:57], v[174:177]
	v_mfma_f32_16x16x128_f8f6f4 v[170:173], v[26:33], v[50:57], v[170:173]
	v_mfma_f32_16x16x128_f8f6f4 v[158:161], v[18:25], v[42:49], v[158:161]
	v_mfma_f32_16x16x128_f8f6f4 v[154:157], v[26:33], v[42:49], v[154:157]
	v_mfma_f32_16x16x128_f8f6f4 v[142:145], v[18:25], v[34:41], v[142:145]
	v_mfma_f32_16x16x128_f8f6f4 v[138:141], v[26:33], v[34:41], v[138:141]
	s_setprio 0
	s_setprio 1
	v_mfma_f32_16x16x128_f8f6f4 v[182:185], v[2:9], v[58:65], v[182:185]
	v_mfma_f32_16x16x128_f8f6f4 v[178:181], v[10:17], v[58:65], v[178:181]
	v_mfma_f32_16x16x128_f8f6f4 v[166:169], v[2:9], v[50:57], v[166:169]
	v_mfma_f32_16x16x128_f8f6f4 v[162:165], v[10:17], v[50:57], v[162:165]
	v_mfma_f32_16x16x128_f8f6f4 v[150:153], v[2:9], v[42:49], v[150:153]
	v_mfma_f32_16x16x128_f8f6f4 v[146:149], v[10:17], v[42:49], v[146:149]
	v_mfma_f32_16x16x128_f8f6f4 v[134:137], v[2:9], v[34:41], v[134:137]
	v_mfma_f32_16x16x128_f8f6f4 v[130:133], v[10:17], v[34:41], v[130:133]
	s_setprio 0
.Lnz_P7a_back:
	s_barrier
	s_mov_b32 m0, s60
	v_lshl_add_u64 v[208:209], s[44:45], 0, v[194:195]
	s_add_u32 s88, s44, 0x20000
	ds_read_b128 v[58:61], v222 offset:16384
	ds_read_b128 v[62:65], v222 offset:16400
	ds_read_b128 v[50:53], v222 offset:18432
	ds_read_b128 v[54:57], v222 offset:18448
	ds_read_b128 v[42:45], v222 offset:20480
	ds_read_b128 v[46:49], v222 offset:20496
	ds_read_b128 v[34:37], v222 offset:22528
	ds_read_b128 v[38:41], v222 offset:22544
	global_load_lds_dwordx4 v[208:209], off
	v_lshl_add_u64 v[206:207], s[44:45], 0, v[196:197]
	s_mov_b32 m0, s61
	s_addc_u32 s89, s45, 0
	global_load_lds_dwordx4 v[206:207], off
	v_lshl_add_u64 v[210:211], s[88:89], 0, v[194:195]
	s_mov_b32 m0, s62
	s_andn2_b64 vcc, exec, s[48:49]
	global_load_lds_dwordx4 v[210:211], off
	v_lshl_add_u64 v[210:211], s[88:89], 0, v[196:197]
	s_mov_b32 m0, s63
	s_nop 0
	global_load_lds_dwordx4 v[210:211], off
	s_mov_b32 m0, s35
	s_nop 0
	global_load_lds_dwordx4 v198, s[46:47]
	s_mov_b32 m0, s64
	s_nop 0
	global_load_lds_dwordx4 v200, s[46:47]
	s_cbranch_vccnz .LBB0_985
	s_waitcnt vmcnt(8)
	s_branch .LBB0_985

.LBB0_1080:
	s_ashr_i32 s57, s56, 31
	s_lshl_b64 s[12:13], s[56:57], 18
	s_add_u32 s12, s70, s12
	s_addc_u32 s13, s71, s13
	s_and_b64 s[28:29], s[0:1], exec
	s_cselect_b32 s57, s13, s51
	s_cselect_b32 s82, s12, s50
	s_lshl_b32 s28, s68, 8
	s_or_b32 s29, s28, 0x80
	s_add_u32 s30, s50, 0x100
	s_addc_u32 s31, s51, 0
	s_mov_b32 s34, -2
	s_mov_b64 s[78:79], s[96:97]
	s_mov_b32 s35, 1
	s_branch .LBB0_1082
.LBB0_1081:
	s_mov_b32 s35, 0
	s_waitcnt lgkmcnt(0)
	v_mov_b32_e32 v201, v199
	v_lshl_add_u64 v[208:209], s[52:53], 0, v[198:199]
	v_lshl_add_u64 v[210:211], s[52:53], 0, v[200:201]
	s_barrier
	s_cmp_eq_u32 s34, -2
	s_cbranch_scc1 .Lnz_P8b_first
	s_setprio 1
	s_waitcnt lgkmcnt(0)
	v_mfma_f32_16x16x128_f8f6f4 v[126:129], v[18:25], v[58:65], v[126:129]
	v_mfma_f32_16x16x128_f8f6f4 v[122:125], v[26:33], v[58:65], v[122:125]
	v_mfma_f32_16x16x128_f8f6f4 v[106:109], v[18:25], v[50:57], v[106:109]
	v_mfma_f32_16x16x128_f8f6f4 v[98:101], v[26:33], v[50:57], v[98:101]
	v_mfma_f32_16x16x128_f8f6f4 v[78:81], v[18:25], v[42:49], v[78:81]
	v_mfma_f32_16x16x128_f8f6f4 v[74:77], v[26:33], v[42:49], v[74:77]
	v_mfma_f32_16x16x128_f8f6f4 v[70:73], v[18:25], v[34:41], v[70:73]
	v_mfma_f32_16x16x128_f8f6f4 v[66:69], v[26:33], v[34:41], v[66:69]
	s_setprio 0
	s_setprio 1
	v_mfma_f32_16x16x128_f8f6f4 v[118:121], v[2:9], v[58:65], v[118:121]
	v_mfma_f32_16x16x128_f8f6f4 v[114:117], v[10:17], v[58:65], v[114:117]
	v_mfma_f32_16x16x128_f8f6f4 v[90:93], v[2:9], v[50:57], v[90:93]
	v_mfma_f32_16x16x128_f8f6f4 v[82:85], v[10:17], v[50:57], v[82:85]
	v_mfma_f32_16x16x128_f8f6f4 v[102:105], v[2:9], v[42:49], v[102:105]
	v_mfma_f32_16x16x128_f8f6f4 v[110:113], v[10:17], v[42:49], v[110:113]
	v_mfma_f32_16x16x128_f8f6f4 v[86:89], v[2:9], v[34:41], v[86:89]
	v_mfma_f32_16x16x128_f8f6f4 v[94:97], v[10:17], v[34:41], v[94:97]
	s_setprio 0
.Lnz_P8b_back:
	s_barrier
	s_add_i32 s54, 0, 0x18000
	s_add_i32 s55, 0, 0x1c000
	v_add_u32_e32 v14, s54, v216
	v_add_u32_e32 v30, s55, v216
	ds_read_b128 v[2:5], v14
	ds_read_b128 v[6:9], v14 offset:16
	ds_read_b128 v[10:13], v14 offset:2048
	ds_read_b128 v[14:17], v14 offset:2064
	ds_read_b128 v[18:21], v30
	ds_read_b128 v[22:25], v30 offset:16
	ds_read_b128 v[26:29], v30 offset:2048
	ds_read_b128 v[30:33], v30 offset:2064
	s_mov_b32 m0, s20
	ds_read_b128 v[34:37], v220 offset:32768
	ds_read_b128 v[38:41], v220 offset:32784
	ds_read_b128 v[42:45], v220 offset:34816
	ds_read_b128 v[46:49], v220 offset:34832
	ds_read_b128 v[50:53], v220 offset:36864
	ds_read_b128 v[54:57], v220 offset:36880
	ds_read_b128 v[58:61], v220 offset:38912
	ds_read_b128 v[62:65], v220 offset:38928
	global_load_lds_dwordx4 v213, s[52:53]
	s_mov_b32 m0, s21
	s_nop 0
	global_load_lds_dwordx4 v214, s[52:53]
	s_waitcnt vmcnt(8)
	s_waitcnt lgkmcnt(0)
	s_barrier
	s_setprio 1
	s_waitcnt lgkmcnt(0)
	v_mfma_f32_16x16x128_f8f6f4 v[190:193], v[2:9], v[34:41], v[190:193]
	v_mfma_f32_16x16x128_f8f6f4 v[186:189], v[10:17], v[34:41], v[186:189]
	v_mfma_f32_16x16x128_f8f6f4 v[182:185], v[2:9], v[42:49], v[182:185]
	v_mfma_f32_16x16x128_f8f6f4 v[178:181], v[10:17], v[42:49], v[178:181]
	v_mfma_f32_16x16x128_f8f6f4 v[158:161], v[2:9], v[50:57], v[158:161]
	v_mfma_f32_16x16x128_f8f6f4 v[154:157], v[10:17], v[50:57], v[154:157]
	v_mfma_f32_16x16x128_f8f6f4 v[142:145], v[2:9], v[58:65], v[142:145]
	v_mfma_f32_16x16x128_f8f6f4 v[138:141], v[10:17], v[58:65], v[138:141]
	s_setprio 0
	s_setprio 1
	v_mfma_f32_16x16x128_f8f6f4 v[174:177], v[18:25], v[34:41], v[174:177]
	v_mfma_f32_16x16x128_f8f6f4 v[170:173], v[26:33], v[34:41], v[170:173]
	v_mfma_f32_16x16x128_f8f6f4 v[166:169], v[18:25], v[42:49], v[166:169]
	v_mfma_f32_16x16x128_f8f6f4 v[162:165], v[26:33], v[42:49], v[162:165]
	v_mfma_f32_16x16x128_f8f6f4 v[150:153], v[18:25], v[50:57], v[150:153]
	v_mfma_f32_16x16x128_f8f6f4 v[146:149], v[26:33], v[50:57], v[146:149]
	v_mfma_f32_16x16x128_f8f6f4 v[134:137], v[18:25], v[58:65], v[134:137]
	v_mfma_f32_16x16x128_f8f6f4 v[130:133], v[26:33], v[58:65], v[130:133]
	s_setprio 0
	s_barrier
	s_add_i32 s52, s54, s69
	v_lshl_add_u64 v[206:207], v[206:207], 0, s[38:39]
	s_mov_b32 m0, s52
	ds_read_b128 v[34:37], v220 offset:49152
	ds_read_b128 v[38:41], v220 offset:49168
	ds_read_b128 v[42:45], v220 offset:51200
	ds_read_b128 v[46:49], v220 offset:51216
	ds_read_b128 v[50:53], v220 offset:53248
	ds_read_b128 v[54:57], v220 offset:53264
	ds_read_b128 v[58:61], v220 offset:55296
	ds_read_b128 v[62:65], v220 offset:55312
	global_load_lds_dwordx4 v[206:207], off
	s_add_i32 m0, s52, 0x2000
	s_add_u32 s50, s50, 0x8080
	v_lshl_add_u64 v[204:205], v[204:205], 0, s[38:39]
	s_addc_u32 s51, s51, 0
	s_add_i32 s52, s55, s69
	global_load_lds_dwordx4 v[204:205], off
	v_lshl_add_u64 v[204:205], s[50:51], 0, v[194:195]
	s_mov_b32 m0, s52
	s_nop 0
	global_load_lds_dwordx4 v[204:205], off
	v_lshl_add_u64 v[204:205], s[50:51], 0, v[196:197]
	s_add_i32 m0, s52, 0x2000
	s_nop 0
	global_load_lds_dwordx4 v[204:205], off
	v_lshl_add_u64 v[204:205], v[208:209], 0, s[38:39]
	s_mov_b32 m0, s22
	s_nop 0
	global_load_lds_dwordx4 v[204:205], off
	v_lshl_add_u64 v[204:205], v[210:211], 0, s[38:39]
	s_mov_b32 m0, s23
	s_nop 0
	global_load_lds_dwordx4 v[204:205], off
	s_waitcnt vmcnt(8)
	s_waitcnt lgkmcnt(0)
	s_barrier
	s_setprio 1
	s_waitcnt lgkmcnt(0)
	v_mfma_f32_16x16x128_f8f6f4 v[126:129], v[2:9], v[34:41], v[126:129]
	v_mfma_f32_16x16x128_f8f6f4 v[122:125], v[10:17], v[34:41], v[122:125]
	v_mfma_f32_16x16x128_f8f6f4 v[106:109], v[2:9], v[42:49], v[106:109]
	v_mfma_f32_16x16x128_f8f6f4 v[98:101], v[10:17], v[42:49], v[98:101]
	v_mfma_f32_16x16x128_f8f6f4 v[78:81], v[2:9], v[50:57], v[78:81]
	v_mfma_f32_16x16x128_f8f6f4 v[74:77], v[10:17], v[50:57], v[74:77]
	v_mfma_f32_16x16x128_f8f6f4 v[70:73], v[2:9], v[58:65], v[70:73]
	v_mfma_f32_16x16x128_f8f6f4 v[66:69], v[10:17], v[58:65], v[66:69]
	s_setprio 0
	s_setprio 1
	v_mfma_f32_16x16x128_f8f6f4 v[118:121], v[18:25], v[34:41], v[118:121]
	v_mfma_f32_16x16x128_f8f6f4 v[114:117], v[26:33], v[34:41], v[114:117]
	v_mfma_f32_16x16x128_f8f6f4 v[90:93], v[18:25], v[42:49], v[90:93]
	v_mfma_f32_16x16x128_f8f6f4 v[82:85], v[26:33], v[42:49], v[82:85]
	v_mfma_f32_16x16x128_f8f6f4 v[102:105], v[18:25], v[50:57], v[102:105]
	v_mfma_f32_16x16x128_f8f6f4 v[110:113], v[26:33], v[50:57], v[110:113]
	v_mfma_f32_16x16x128_f8f6f4 v[86:89], v[18:25], v[58:65], v[86:89]
	v_mfma_f32_16x16x128_f8f6f4 v[94:97], v[26:33], v[58:65], v[94:97]
	s_setprio 0
	s_barrier
	s_add_i32 s34, s34, 2
	s_add_u32 s78, s78, 0x100
	s_addc_u32 s79, s79, 0
	s_add_u32 s30, s30, 0x100
	s_addc_u32 s31, s31, 0
	s_cmp_gt_u32 s34, 5
	s_cbranch_scc1 .LBB0_1088

.LBB0_1086:
	s_add_u32 s35, s78, 0x80
	s_addc_u32 s52, s79, 0
	s_waitcnt lgkmcnt(0)
	s_and_b64 s[50:51], s[50:51], exec
	s_cselect_b32 s53, s59, s52
	s_cselect_b32 s52, s58, s35
	s_cselect_b32 s51, s57, s31
	s_cselect_b32 s50, s82, s30
	s_barrier
	s_cmp_eq_u32 s34, -2
	s_cbranch_scc1 .Lnz_P8a_first
	s_setprio 1
	s_waitcnt lgkmcnt(0)
	v_mfma_f32_16x16x128_f8f6f4 v[190:193], v[18:25], v[58:65], v[190:193]
	v_mfma_f32_16x16x128_f8f6f4 v[186:189], v[26:33], v[58:65], v[186:189]
	v_mfma_f32_16x16x128_f8f6f4 v[182:185], v[18:25], v[50:57], v[182:185]
	v_mfma_f32_16x16x128_f8f6f4 v[178:181], v[26:33], v[50:57], v[178:181]
	v_mfma_f32_16x16x128_f8f6f4 v[158:161], v[18:25], v[42:49], v[158:161]
	v_mfma_f32_16x16x128_f8f6f4 v[154:157], v[26:33], v[42:49], v[154:157]
	v_mfma_f32_16x16x128_f8f6f4 v[142:145], v[18:25], v[34:41], v[142:145]
	v_mfma_f32_16x16x128_f8f6f4 v[138:141], v[26:33], v[34:41], v[138:141]
	s_setprio 0
	s_setprio 1
	v_mfma_f32_16x16x128_f8f6f4 v[174:177], v[2:9], v[58:65], v[174:177]
	v_mfma_f32_16x16x128_f8f6f4 v[170:173], v[10:17], v[58:65], v[170:173]
	v_mfma_f32_16x16x128_f8f6f4 v[166:169], v[2:9], v[50:57], v[166:169]
	v_mfma_f32_16x16x128_f8f6f4 v[162:165], v[10:17], v[50:57], v[162:165]
	v_mfma_f32_16x16x128_f8f6f4 v[150:153], v[2:9], v[42:49], v[150:153]
	v_mfma_f32_16x16x128_f8f6f4 v[146:149], v[10:17], v[42:49], v[146:149]
	v_mfma_f32_16x16x128_f8f6f4 v[134:137], v[2:9], v[34:41], v[134:137]
	v_mfma_f32_16x16x128_f8f6f4 v[130:133], v[10:17], v[34:41], v[130:133]
	s_setprio 0
.Lnz_P8a_back:
	s_barrier
	s_mov_b32 m0, s15
	v_lshl_add_u64 v[206:207], s[50:51], 0, v[194:195]
	s_add_u32 vcc_lo, s50, 0x8000
	ds_read_b128 v[58:61], v220 offset:16384
	ds_read_b128 v[62:65], v220 offset:16400
	ds_read_b128 v[50:53], v220 offset:18432
	ds_read_b128 v[54:57], v220 offset:18448
	ds_read_b128 v[42:45], v220 offset:20480
	ds_read_b128 v[46:49], v220 offset:20496
	ds_read_b128 v[34:37], v220 offset:22528
	ds_read_b128 v[38:41], v220 offset:22544
	global_load_lds_dwordx4 v[206:207], off
	v_lshl_add_u64 v[204:205], s[50:51], 0, v[196:197]
	s_mov_b32 m0, s16
	s_addc_u32 vcc_hi, s51, 0
	global_load_lds_dwordx4 v[204:205], off
	v_lshl_add_u64 v[208:209], vcc, 0, v[194:195]
	s_mov_b32 m0, s17
	s_nop 0
	global_load_lds_dwordx4 v[208:209], off
	v_lshl_add_u64 v[208:209], vcc, 0, v[196:197]
	s_mov_b32 m0, s18
	s_andn2_b64 vcc, exec, s[54:55]
	global_load_lds_dwordx4 v[208:209], off
	s_mov_b32 m0, s14
	s_nop 0
	global_load_lds_dwordx4 v198, s[52:53]
	s_mov_b32 m0, s19
	s_nop 0
	global_load_lds_dwordx4 v200, s[52:53]
	s_cbranch_vccnz .LBB0_1081
	s_waitcnt vmcnt(8)
	s_branch .LBB0_1081

.Lnz_P1a_first:
	s_setprio 1
	s_waitcnt lgkmcnt(0)
	v_mfma_f32_16x16x128_f8f6f4 v[190:193], v[18:25], v[58:65], 0
	v_mfma_f32_16x16x128_f8f6f4 v[186:189], v[26:33], v[58:65], 0
	v_mfma_f32_16x16x128_f8f6f4 v[174:177], v[18:25], v[50:57], 0
	v_mfma_f32_16x16x128_f8f6f4 v[170:173], v[26:33], v[50:57], 0
	v_mfma_f32_16x16x128_f8f6f4 v[158:161], v[18:25], v[42:49], 0
	v_mfma_f32_16x16x128_f8f6f4 v[154:157], v[26:33], v[42:49], 0
	v_mfma_f32_16x16x128_f8f6f4 v[142:145], v[18:25], v[34:41], 0
	v_mfma_f32_16x16x128_f8f6f4 v[138:141], v[26:33], v[34:41], 0
	s_setprio 0
	s_setprio 1
	v_mfma_f32_16x16x128_f8f6f4 v[182:185], v[2:9], v[58:65], 0
	v_mfma_f32_16x16x128_f8f6f4 v[178:181], v[10:17], v[58:65], 0
	v_mfma_f32_16x16x128_f8f6f4 v[166:169], v[2:9], v[50:57], 0
	v_mfma_f32_16x16x128_f8f6f4 v[162:165], v[10:17], v[50:57], 0
	v_mfma_f32_16x16x128_f8f6f4 v[150:153], v[2:9], v[42:49], 0
	v_mfma_f32_16x16x128_f8f6f4 v[146:149], v[10:17], v[42:49], 0
	v_mfma_f32_16x16x128_f8f6f4 v[134:137], v[2:9], v[34:41], 0
	v_mfma_f32_16x16x128_f8f6f4 v[130:133], v[10:17], v[34:41], 0
	s_setprio 0
	s_branch .Lnz_P1a_back
.Lnz_P1b_first:
	s_setprio 1
	s_waitcnt lgkmcnt(0)
	v_mfma_f32_16x16x128_f8f6f4 v[126:129], v[18:25], v[58:65], 0
	v_mfma_f32_16x16x128_f8f6f4 v[122:125], v[26:33], v[58:65], 0
	v_mfma_f32_16x16x128_f8f6f4 v[110:113], v[18:25], v[50:57], 0
	v_mfma_f32_16x16x128_f8f6f4 v[106:109], v[26:33], v[50:57], 0
	v_mfma_f32_16x16x128_f8f6f4 v[78:81], v[18:25], v[42:49], 0
	v_mfma_f32_16x16x128_f8f6f4 v[74:77], v[26:33], v[42:49], 0
	v_mfma_f32_16x16x128_f8f6f4 v[70:73], v[18:25], v[34:41], 0
	v_mfma_f32_16x16x128_f8f6f4 v[66:69], v[26:33], v[34:41], 0
	s_setprio 0
	s_setprio 1
	v_mfma_f32_16x16x128_f8f6f4 v[118:121], v[2:9], v[58:65], 0
	v_mfma_f32_16x16x128_f8f6f4 v[114:117], v[10:17], v[58:65], 0
	v_mfma_f32_16x16x128_f8f6f4 v[94:97], v[2:9], v[50:57], 0
	v_mfma_f32_16x16x128_f8f6f4 v[90:93], v[10:17], v[50:57], 0
	v_mfma_f32_16x16x128_f8f6f4 v[98:101], v[2:9], v[42:49], 0
	v_mfma_f32_16x16x128_f8f6f4 v[102:105], v[10:17], v[42:49], 0
	v_mfma_f32_16x16x128_f8f6f4 v[82:85], v[2:9], v[34:41], 0
	v_mfma_f32_16x16x128_f8f6f4 v[86:89], v[10:17], v[34:41], 0
	s_setprio 0
	s_branch .Lnz_P1b_back

.Lnz_P4b_first:
	s_setprio 1
	s_waitcnt lgkmcnt(0)
	v_mfma_f32_16x16x128_f8f6f4 v[126:129], v[18:25], v[58:65], 0
	v_mfma_f32_16x16x128_f8f6f4 v[122:125], v[26:33], v[58:65], 0
	v_mfma_f32_16x16x128_f8f6f4 v[110:113], v[18:25], v[50:57], 0
	v_mfma_f32_16x16x128_f8f6f4 v[106:109], v[26:33], v[50:57], 0
	v_mfma_f32_16x16x128_f8f6f4 v[86:89], v[18:25], v[42:49], 0
	v_mfma_f32_16x16x128_f8f6f4 v[82:85], v[26:33], v[42:49], 0
	v_mfma_f32_16x16x128_f8f6f4 v[70:73], v[18:25], v[34:41], 0
	v_mfma_f32_16x16x128_f8f6f4 v[66:69], v[26:33], v[34:41], 0
	s_setprio 0
	s_setprio 1
	v_mfma_f32_16x16x128_f8f6f4 v[118:121], v[2:9], v[58:65], 0
	v_mfma_f32_16x16x128_f8f6f4 v[114:117], v[10:17], v[58:65], 0
	v_mfma_f32_16x16x128_f8f6f4 v[102:105], v[2:9], v[50:57], 0
	v_mfma_f32_16x16x128_f8f6f4 v[90:93], v[10:17], v[50:57], 0
	v_mfma_f32_16x16x128_f8f6f4 v[98:101], v[2:9], v[42:49], 0
	v_mfma_f32_16x16x128_f8f6f4 v[94:97], v[10:17], v[42:49], 0
	v_mfma_f32_16x16x128_f8f6f4 v[78:81], v[2:9], v[34:41], 0
	v_mfma_f32_16x16x128_f8f6f4 v[74:77], v[10:17], v[34:41], 0
	s_setprio 0
	s_branch .Lnz_P4b_back

.Lnz_P7b_first:
	s_setprio 1
	s_waitcnt lgkmcnt(0)
	v_mfma_f32_16x16x128_f8f6f4 v[126:129], v[18:25], v[58:65], 0
	v_mfma_f32_16x16x128_f8f6f4 v[122:125], v[26:33], v[58:65], 0
	v_mfma_f32_16x16x128_f8f6f4 v[110:113], v[18:25], v[50:57], 0
	v_mfma_f32_16x16x128_f8f6f4 v[106:109], v[26:33], v[50:57], 0
	v_mfma_f32_16x16x128_f8f6f4 v[86:89], v[18:25], v[42:49], 0
	v_mfma_f32_16x16x128_f8f6f4 v[82:85], v[26:33], v[42:49], 0
	v_mfma_f32_16x16x128_f8f6f4 v[70:73], v[18:25], v[34:41], 0
	v_mfma_f32_16x16x128_f8f6f4 v[66:69], v[26:33], v[34:41], 0
	s_setprio 0
	s_setprio 1
	v_mfma_f32_16x16x128_f8f6f4 v[118:121], v[2:9], v[58:65], 0
	v_mfma_f32_16x16x128_f8f6f4 v[114:117], v[10:17], v[58:65], 0
	v_mfma_f32_16x16x128_f8f6f4 v[102:105], v[2:9], v[50:57], 0
	v_mfma_f32_16x16x128_f8f6f4 v[90:93], v[10:17], v[50:57], 0
	v_mfma_f32_16x16x128_f8f6f4 v[94:97], v[2:9], v[42:49], 0
	v_mfma_f32_16x16x128_f8f6f4 v[98:101], v[10:17], v[42:49], 0
	v_mfma_f32_16x16x128_f8f6f4 v[74:77], v[2:9], v[34:41], 0
	v_mfma_f32_16x16x128_f8f6f4 v[78:81], v[10:17], v[34:41], 0
	s_setprio 0
	s_branch .Lnz_P7b_back
.Lnz_P8a_first:
	s_setprio 1
	s_waitcnt lgkmcnt(0)
	v_mfma_f32_16x16x128_f8f6f4 v[190:193], v[18:25], v[58:65], 0
	v_mfma_f32_16x16x128_f8f6f4 v[186:189], v[26:33], v[58:65], 0
	v_mfma_f32_16x16x128_f8f6f4 v[182:185], v[18:25], v[50:57], 0
	v_mfma_f32_16x16x128_f8f6f4 v[178:181], v[26:33], v[50:57], 0
	v_mfma_f32_16x16x128_f8f6f4 v[158:161], v[18:25], v[42:49], 0
	v_mfma_f32_16x16x128_f8f6f4 v[154:157], v[26:33], v[42:49], 0
	v_mfma_f32_16x16x128_f8f6f4 v[142:145], v[18:25], v[34:41], 0
	v_mfma_f32_16x16x128_f8f6f4 v[138:141], v[26:33], v[34:41], 0
	s_setprio 0
	s_setprio 1
	v_mfma_f32_16x16x128_f8f6f4 v[174:177], v[2:9], v[58:65], 0
	v_mfma_f32_16x16x128_f8f6f4 v[170:173], v[10:17], v[58:65], 0
	v_mfma_f32_16x16x128_f8f6f4 v[166:169], v[2:9], v[50:57], 0
	v_mfma_f32_16x16x128_f8f6f4 v[162:165], v[10:17], v[50:57], 0
	v_mfma_f32_16x16x128_f8f6f4 v[150:153], v[2:9], v[42:49], 0
	v_mfma_f32_16x16x128_f8f6f4 v[146:149], v[10:17], v[42:49], 0
	v_mfma_f32_16x16x128_f8f6f4 v[134:137], v[2:9], v[34:41], 0
	v_mfma_f32_16x16x128_f8f6f4 v[130:133], v[10:17], v[34:41], 0
	s_setprio 0
	s_branch .Lnz_P8a_back
.Lnz_P8b_first:
	s_setprio 1
	s_waitcnt lgkmcnt(0)
	v_mfma_f32_16x16x128_f8f6f4 v[126:129], v[18:25], v[58:65], 0
	v_mfma_f32_16x16x128_f8f6f4 v[122:125], v[26:33], v[58:65], 0
	v_mfma_f32_16x16x128_f8f6f4 v[106:109], v[18:25], v[50:57], 0
	v_mfma_f32_16x16x128_f8f6f4 v[98:101], v[26:33], v[50:57], 0
	v_mfma_f32_16x16x128_f8f6f4 v[78:81], v[18:25], v[42:49], 0
	v_mfma_f32_16x16x128_f8f6f4 v[74:77], v[26:33], v[42:49], 0
	v_mfma_f32_16x16x128_f8f6f4 v[70:73], v[18:25], v[34:41], 0
	v_mfma_f32_16x16x128_f8f6f4 v[66:69], v[26:33], v[34:41], 0
	s_setprio 0
	s_setprio 1
	v_mfma_f32_16x16x128_f8f6f4 v[118:121], v[2:9], v[58:65], 0
	v_mfma_f32_16x16x128_f8f6f4 v[114:117], v[10:17], v[58:65], 0
	v_mfma_f32_16x16x128_f8f6f4 v[90:93], v[2:9], v[50:57], 0
	v_mfma_f32_16x16x128_f8f6f4 v[82:85], v[10:17], v[50:57], 0
	v_mfma_f32_16x16x128_f8f6f4 v[102:105], v[2:9], v[42:49], 0
	v_mfma_f32_16x16x128_f8f6f4 v[110:113], v[10:17], v[42:49], 0
	v_mfma_f32_16x16x128_f8f6f4 v[86:89], v[2:9], v[34:41], 0
	v_mfma_f32_16x16x128_f8f6f4 v[94:97], v[10:17], v[34:41], 0
	s_setprio 0
	s_branch .Lnz_P8b_back
